# waitcnt placement: compiler's s_waitcnt vmcnt(0) hoisted out of the out-proj and MoE-down K-loops into their preheaders (counted vmcnt(8) waits remain)
# baseline (speedup 1.0000x reference)
.LBB0_990:
	s_add_u32 s18, s62, s14
	s_addc_u32 s19, s63, s15
	s_and_b64 s[28:29], s[38:39], exec
	s_cselect_b32 s11, s19, s41
	s_cselect_b32 s13, s18, s40
	s_add_u32 s30, s4, s16
	s_addc_u32 s31, s24, s17
	s_and_b64 s[28:29], s[38:39], exec
	s_cselect_b32 s60, s31, s43
	s_cselect_b32 s61, s30, s42
	s_add_u32 s40, s40, 0x80080
	s_addc_u32 s41, s41, 0
	s_add_u32 s62, s42, 0x100
	v_mov_b32_e32 v0, 0
	s_addc_u32 s63, s43, 0
	s_mov_b32 s79, -2
	v_mov_b32_e32 v1, v0
	v_mov_b32_e32 v2, v0
	v_mov_b32_e32 v3, v0
	v_mov_b32_e32 v4, v0
	v_mov_b32_e32 v5, v0
	v_mov_b32_e32 v6, v0
	v_mov_b32_e32 v7, v0
	v_mov_b32_e32 v16, v0
	v_mov_b32_e32 v17, v0
	v_mov_b32_e32 v18, v0
	v_mov_b32_e32 v19, v0
	v_mov_b32_e32 v20, v0
	v_mov_b32_e32 v21, v0
	v_mov_b32_e32 v22, v0
	v_mov_b32_e32 v23, v0
	v_mov_b32_e32 v32, v0
	v_mov_b32_e32 v33, v0
	v_mov_b32_e32 v34, v0
	v_mov_b32_e32 v35, v0
	v_mov_b32_e32 v36, v0
	v_mov_b32_e32 v37, v0
	v_mov_b32_e32 v38, v0
	v_mov_b32_e32 v39, v0
	v_mov_b32_e32 v64, v0
	v_mov_b32_e32 v65, v0
	v_mov_b32_e32 v66, v0
	v_mov_b32_e32 v67, v0
	v_mov_b32_e32 v68, v0
	v_mov_b32_e32 v69, v0
	v_mov_b32_e32 v70, v0
	v_mov_b32_e32 v71, v0
	v_mov_b32_e32 v8, v0
	v_mov_b32_e32 v9, v0
	v_mov_b32_e32 v10, v0
	v_mov_b32_e32 v11, v0
	v_mov_b32_e32 v12, v0
	v_mov_b32_e32 v13, v0
	v_mov_b32_e32 v14, v0
	v_mov_b32_e32 v15, v0
	v_mov_b32_e32 v24, v0
	v_mov_b32_e32 v25, v0
	v_mov_b32_e32 v26, v0
	v_mov_b32_e32 v27, v0
	v_mov_b32_e32 v28, v0
	v_mov_b32_e32 v29, v0
	v_mov_b32_e32 v30, v0
	v_mov_b32_e32 v31, v0
	v_mov_b32_e32 v48, v0
	v_mov_b32_e32 v49, v0
	v_mov_b32_e32 v50, v0
	v_mov_b32_e32 v51, v0
	v_mov_b32_e32 v52, v0
	v_mov_b32_e32 v53, v0
	v_mov_b32_e32 v54, v0
	v_mov_b32_e32 v55, v0
	v_mov_b32_e32 v72, v0
	v_mov_b32_e32 v73, v0
	v_mov_b32_e32 v74, v0
	v_mov_b32_e32 v75, v0
	v_mov_b32_e32 v76, v0
	v_mov_b32_e32 v77, v0
	v_mov_b32_e32 v78, v0
	v_mov_b32_e32 v79, v0
	v_mov_b32_e32 v80, v0
	v_mov_b32_e32 v81, v0
	v_mov_b32_e32 v82, v0
	v_mov_b32_e32 v83, v0
	v_mov_b32_e32 v84, v0
	v_mov_b32_e32 v85, v0
	v_mov_b32_e32 v86, v0
	v_mov_b32_e32 v87, v0
	v_mov_b32_e32 v96, v0
	v_mov_b32_e32 v97, v0
	v_mov_b32_e32 v98, v0
	v_mov_b32_e32 v99, v0
	v_mov_b32_e32 v100, v0
	v_mov_b32_e32 v101, v0
	v_mov_b32_e32 v102, v0
	v_mov_b32_e32 v103, v0
	v_mov_b32_e32 v112, v0
	v_mov_b32_e32 v113, v0
	v_mov_b32_e32 v114, v0
	v_mov_b32_e32 v115, v0
	v_mov_b32_e32 v116, v0
	v_mov_b32_e32 v117, v0
	v_mov_b32_e32 v118, v0
	v_mov_b32_e32 v119, v0
	v_mov_b32_e32 v128, v0
	v_mov_b32_e32 v129, v0
	v_mov_b32_e32 v130, v0
	v_mov_b32_e32 v131, v0
	v_mov_b32_e32 v132, v0
	v_mov_b32_e32 v133, v0
	v_mov_b32_e32 v134, v0
	v_mov_b32_e32 v135, v0
	v_mov_b32_e32 v88, v0
	v_mov_b32_e32 v89, v0
	v_mov_b32_e32 v90, v0
	v_mov_b32_e32 v91, v0
	v_mov_b32_e32 v92, v0
	v_mov_b32_e32 v93, v0
	v_mov_b32_e32 v94, v0
	v_mov_b32_e32 v95, v0
	v_mov_b32_e32 v104, v0
	v_mov_b32_e32 v105, v0
	v_mov_b32_e32 v106, v0
	v_mov_b32_e32 v107, v0
	v_mov_b32_e32 v108, v0
	v_mov_b32_e32 v109, v0
	v_mov_b32_e32 v110, v0
	v_mov_b32_e32 v111, v0
	v_mov_b32_e32 v120, v0
	v_mov_b32_e32 v121, v0
	v_mov_b32_e32 v122, v0
	v_mov_b32_e32 v123, v0
	v_mov_b32_e32 v124, v0
	v_mov_b32_e32 v125, v0
	v_mov_b32_e32 v126, v0
	v_mov_b32_e32 v127, v0
	v_mov_b32_e32 v136, v0
	v_mov_b32_e32 v137, v0
	v_mov_b32_e32 v138, v0
	v_mov_b32_e32 v139, v0
	v_mov_b32_e32 v140, v0
	v_mov_b32_e32 v141, v0
	v_mov_b32_e32 v142, v0
	v_mov_b32_e32 v143, v0
	s_waitcnt vmcnt(0)
.LBB0_991:
	s_add_u32 s28, s40, 0xfff80080
	s_addc_u32 s29, s41, -1
	s_add_i32 s48, 0, 0x10000
	s_cmp_eq_u32 s79, 28
	s_cselect_b32 s45, s11, s29
	s_cselect_b32 s44, s13, s28
	s_cselect_b32 s43, s60, s63
	s_cselect_b32 s42, s61, s62
	s_add_i32 s49, 0, 0x14000
	v_add_u32_e32 v60, s48, v169
	v_add_u32_e32 v166, s49, v169
	ds_read_b128 v[40:43], v60
	ds_read_b128 v[44:47], v60 offset:1024
	ds_read_b128 v[56:59], v60 offset:2048
	ds_read_b128 v[60:63], v60 offset:3072
	ds_read_b128 v[144:147], v166
	ds_read_b128 v[148:151], v166 offset:1024
	ds_read_b128 v[162:165], v166 offset:2048
	ds_read_b128 v[172:175], v166 offset:3072
	v_lshl_add_u64 v[166:167], s[40:41], 0, v[158:159]
	s_add_i32 m0, s26, 0xc000
	ds_read_b128 v[176:179], v171
	ds_read_b128 v[180:183], v171 offset:1024
	ds_read_b128 v[194:197], v171 offset:2048
	ds_read_b128 v[198:201], v171 offset:3072
	ds_read_b128 v[202:205], v171 offset:4096
	ds_read_b128 v[206:209], v171 offset:5120
	ds_read_b128 v[224:227], v171 offset:6144
	ds_read_b128 v[228:231], v171 offset:7168
	global_load_lds_dwordx4 v[166:167], off
	v_lshl_add_u64 v[166:167], s[40:41], 0, v[160:161]
	s_add_i32 m0, s26, 0xe000
	s_nop 0
	global_load_lds_dwordx4 v[166:167], off
	s_waitcnt vmcnt(8)
	s_waitcnt lgkmcnt(0)
	s_barrier
	s_setprio 1
	s_waitcnt lgkmcnt(0)
	v_mfma_f32_16x16x32_bf16 v[140:143], v[40:43], v[176:179], v[140:143]
	v_mfma_f32_16x16x32_bf16 v[136:139], v[56:59], v[176:179], v[136:139]
	v_mfma_f32_16x16x32_bf16 v[124:127], v[40:43], v[194:197], v[124:127]
	v_mfma_f32_16x16x32_bf16 v[120:123], v[56:59], v[194:197], v[120:123]
	v_mfma_f32_16x16x32_bf16 v[108:111], v[40:43], v[202:205], v[108:111]
	v_mfma_f32_16x16x32_bf16 v[104:107], v[56:59], v[202:205], v[104:107]
	v_mfma_f32_16x16x32_bf16 v[92:95], v[40:43], v[224:227], v[92:95]
	v_mfma_f32_16x16x32_bf16 v[88:91], v[56:59], v[224:227], v[88:91]
	v_mfma_f32_16x16x32_bf16 v[140:143], v[44:47], v[180:183], v[140:143]
	v_mfma_f32_16x16x32_bf16 v[136:139], v[60:63], v[180:183], v[136:139]
	v_mfma_f32_16x16x32_bf16 v[124:127], v[44:47], v[198:201], v[124:127]
	v_mfma_f32_16x16x32_bf16 v[120:123], v[60:63], v[198:201], v[120:123]
	v_mfma_f32_16x16x32_bf16 v[108:111], v[44:47], v[206:209], v[108:111]
	v_mfma_f32_16x16x32_bf16 v[104:107], v[60:63], v[206:209], v[104:107]
	v_mfma_f32_16x16x32_bf16 v[92:95], v[44:47], v[228:231], v[92:95]
	v_mfma_f32_16x16x32_bf16 v[88:91], v[60:63], v[228:231], v[88:91]
	s_setprio 0
	s_setprio 1
	v_mfma_f32_16x16x32_bf16 v[132:135], v[144:147], v[176:179], v[132:135]
	v_mfma_f32_16x16x32_bf16 v[128:131], v[162:165], v[176:179], v[128:131]
	v_mfma_f32_16x16x32_bf16 v[116:119], v[144:147], v[194:197], v[116:119]
	v_mfma_f32_16x16x32_bf16 v[112:115], v[162:165], v[194:197], v[112:115]
	v_mfma_f32_16x16x32_bf16 v[100:103], v[144:147], v[202:205], v[100:103]
	v_mfma_f32_16x16x32_bf16 v[96:99], v[162:165], v[202:205], v[96:99]
	v_mfma_f32_16x16x32_bf16 v[84:87], v[144:147], v[224:227], v[84:87]
	v_mfma_f32_16x16x32_bf16 v[80:83], v[162:165], v[224:227], v[80:83]
	v_mfma_f32_16x16x32_bf16 v[132:135], v[148:151], v[180:183], v[132:135]
	v_mfma_f32_16x16x32_bf16 v[128:131], v[172:175], v[180:183], v[128:131]
	v_mfma_f32_16x16x32_bf16 v[116:119], v[148:151], v[198:201], v[116:119]
	v_mfma_f32_16x16x32_bf16 v[112:115], v[172:175], v[198:201], v[112:115]
	v_mfma_f32_16x16x32_bf16 v[100:103], v[148:151], v[206:209], v[100:103]
	v_mfma_f32_16x16x32_bf16 v[96:99], v[172:175], v[206:209], v[96:99]
	v_mfma_f32_16x16x32_bf16 v[84:87], v[148:151], v[228:231], v[84:87]
	v_mfma_f32_16x16x32_bf16 v[80:83], v[172:175], v[228:231], v[80:83]
	s_setprio 0
	s_barrier
	s_add_i32 s28, s48, s46
	v_lshl_add_u64 v[166:167], s[42:43], 0, v[184:185]
	s_mov_b32 m0, s28
	ds_read_b128 v[176:179], v171 offset:16384
	ds_read_b128 v[180:183], v171 offset:17408
	ds_read_b128 v[194:197], v171 offset:18432
	ds_read_b128 v[198:201], v171 offset:19456
	ds_read_b128 v[202:205], v171 offset:20480
	ds_read_b128 v[206:209], v171 offset:21504
	ds_read_b128 v[224:227], v171 offset:22528
	ds_read_b128 v[228:231], v171 offset:23552
	global_load_lds_dwordx4 v[166:167], off
	s_add_i32 m0, s28, 0x2000
	s_add_u32 s28, s42, 0x80000
	v_lshl_add_u64 v[210:211], s[42:43], 0, v[152:153]
	s_addc_u32 s29, s43, 0
	s_add_i32 s48, s49, s46
	global_load_lds_dwordx4 v[210:211], off
	v_lshl_add_u64 v[216:217], s[28:29], 0, v[184:185]
	s_mov_b32 m0, s48
	v_lshl_add_u64 v[218:219], s[44:45], 0, v[154:155]
	global_load_lds_dwordx4 v[216:217], off
	v_lshl_add_u64 v[216:217], s[28:29], 0, v[152:153]
	s_add_i32 m0, s48, 0x2000
	s_nop 0
	global_load_lds_dwordx4 v[216:217], off
	v_lshl_add_u64 v[216:217], s[44:45], 0, v[156:157]
	s_mov_b32 m0, s26
	s_nop 0
	global_load_lds_dwordx4 v[216:217], off
	s_mov_b32 m0, s27
	s_nop 0
	global_load_lds_dwordx4 v[218:219], off
	s_waitcnt vmcnt(8)
	s_waitcnt lgkmcnt(0)
	s_barrier
	s_setprio 1
	s_waitcnt lgkmcnt(0)
	v_mfma_f32_16x16x32_bf16 v[76:79], v[40:43], v[176:179], v[76:79]
	v_mfma_f32_16x16x32_bf16 v[72:75], v[56:59], v[176:179], v[72:75]
	v_mfma_f32_16x16x32_bf16 v[52:55], v[40:43], v[194:197], v[52:55]
	v_mfma_f32_16x16x32_bf16 v[48:51], v[56:59], v[194:197], v[48:51]
	v_mfma_f32_16x16x32_bf16 v[28:31], v[40:43], v[202:205], v[28:31]
	v_mfma_f32_16x16x32_bf16 v[24:27], v[56:59], v[202:205], v[24:27]
	v_mfma_f32_16x16x32_bf16 v[12:15], v[40:43], v[224:227], v[12:15]
	v_mfma_f32_16x16x32_bf16 v[8:11], v[56:59], v[224:227], v[8:11]
	v_mfma_f32_16x16x32_bf16 v[76:79], v[44:47], v[180:183], v[76:79]
	v_mfma_f32_16x16x32_bf16 v[72:75], v[60:63], v[180:183], v[72:75]
	v_mfma_f32_16x16x32_bf16 v[52:55], v[44:47], v[198:201], v[52:55]
	v_mfma_f32_16x16x32_bf16 v[48:51], v[60:63], v[198:201], v[48:51]
	v_mfma_f32_16x16x32_bf16 v[28:31], v[44:47], v[206:209], v[28:31]
	v_mfma_f32_16x16x32_bf16 v[24:27], v[60:63], v[206:209], v[24:27]
	v_mfma_f32_16x16x32_bf16 v[12:15], v[44:47], v[228:231], v[12:15]
	v_mfma_f32_16x16x32_bf16 v[8:11], v[60:63], v[228:231], v[8:11]
	s_setprio 0
	s_setprio 1
	v_mfma_f32_16x16x32_bf16 v[36:39], v[144:147], v[194:197], v[36:39]
	v_mfma_f32_16x16x32_bf16 v[32:35], v[162:165], v[194:197], v[32:35]
	v_mfma_f32_16x16x32_bf16 v[20:23], v[144:147], v[202:205], v[20:23]
	v_mfma_f32_16x16x32_bf16 v[16:19], v[162:165], v[202:205], v[16:19]
	v_mfma_f32_16x16x32_bf16 v[4:7], v[144:147], v[224:227], v[4:7]
	v_mfma_f32_16x16x32_bf16 v[0:3], v[162:165], v[224:227], v[0:3]
	v_mfma_f32_16x16x32_bf16 v[40:43], v[144:147], v[176:179], v[68:71]
	v_mfma_f32_16x16x32_bf16 v[44:47], v[162:165], v[176:179], v[64:67]
	v_mfma_f32_16x16x32_bf16 v[36:39], v[148:151], v[198:201], v[36:39]
	v_mfma_f32_16x16x32_bf16 v[32:35], v[172:175], v[198:201], v[32:35]
	v_mfma_f32_16x16x32_bf16 v[20:23], v[148:151], v[206:209], v[20:23]
	v_mfma_f32_16x16x32_bf16 v[16:19], v[172:175], v[206:209], v[16:19]
	v_mfma_f32_16x16x32_bf16 v[4:7], v[148:151], v[228:231], v[4:7]
	v_mfma_f32_16x16x32_bf16 v[0:3], v[172:175], v[228:231], v[0:3]
	v_mfma_f32_16x16x32_bf16 v[40:43], v[148:151], v[180:183], v[40:43]
	v_mfma_f32_16x16x32_bf16 v[44:47], v[172:175], v[180:183], v[44:47]
	s_setprio 0
	s_barrier
	s_add_i32 s48, 0, 0x18000
	s_add_i32 s49, 0, 0x1c000
	v_add_u32_e32 v68, s48, v169
	v_add_u32_e32 v172, s49, v169
	ds_read_b128 v[56:59], v68
	ds_read_b128 v[60:63], v68 offset:1024
	ds_read_b128 v[64:67], v68 offset:2048
	ds_read_b128 v[68:71], v68 offset:3072
	ds_read_b128 v[144:147], v172
	ds_read_b128 v[148:151], v172 offset:1024
	ds_read_b128 v[162:165], v172 offset:2048
	ds_read_b128 v[172:175], v172 offset:3072
	s_add_u32 s28, s44, 0x80000
	s_addc_u32 s29, s45, 0
	s_mov_b32 m0, s47
	v_lshl_add_u64 v[232:233], s[28:29], 0, v[156:157]
	ds_read_b128 v[176:179], v171 offset:32768
	ds_read_b128 v[180:183], v171 offset:33792
	ds_read_b128 v[194:197], v171 offset:34816
	ds_read_b128 v[198:201], v171 offset:35840
	ds_read_b128 v[202:205], v171 offset:36864
	ds_read_b128 v[206:209], v171 offset:37888
	ds_read_b128 v[224:227], v171 offset:38912
	ds_read_b128 v[228:231], v171 offset:39936
	global_load_lds_dwordx4 v[232:233], off
	v_lshl_add_u64 v[232:233], s[28:29], 0, v[154:155]
	s_mov_b32 m0, s50
	s_nop 0
	global_load_lds_dwordx4 v[232:233], off
	s_waitcnt vmcnt(8)
	s_waitcnt lgkmcnt(0)
	s_barrier
	s_setprio 1
	s_waitcnt lgkmcnt(0)
	v_mfma_f32_16x16x32_bf16 v[140:143], v[56:59], v[176:179], v[140:143]
	v_mfma_f32_16x16x32_bf16 v[136:139], v[64:67], v[176:179], v[136:139]
	v_mfma_f32_16x16x32_bf16 v[124:127], v[56:59], v[194:197], v[124:127]
	v_mfma_f32_16x16x32_bf16 v[120:123], v[64:67], v[194:197], v[120:123]
	v_mfma_f32_16x16x32_bf16 v[108:111], v[56:59], v[202:205], v[108:111]
	v_mfma_f32_16x16x32_bf16 v[104:107], v[64:67], v[202:205], v[104:107]
	v_mfma_f32_16x16x32_bf16 v[92:95], v[56:59], v[224:227], v[92:95]
	v_mfma_f32_16x16x32_bf16 v[88:91], v[64:67], v[224:227], v[88:91]
	v_mfma_f32_16x16x32_bf16 v[140:143], v[60:63], v[180:183], v[140:143]
	v_mfma_f32_16x16x32_bf16 v[136:139], v[68:71], v[180:183], v[136:139]
	v_mfma_f32_16x16x32_bf16 v[124:127], v[60:63], v[198:201], v[124:127]
	v_mfma_f32_16x16x32_bf16 v[120:123], v[68:71], v[198:201], v[120:123]
	v_mfma_f32_16x16x32_bf16 v[108:111], v[60:63], v[206:209], v[108:111]
	v_mfma_f32_16x16x32_bf16 v[104:107], v[68:71], v[206:209], v[104:107]
	v_mfma_f32_16x16x32_bf16 v[92:95], v[60:63], v[228:231], v[92:95]
	v_mfma_f32_16x16x32_bf16 v[88:91], v[68:71], v[228:231], v[88:91]
	s_setprio 0
	s_setprio 1
	v_mfma_f32_16x16x32_bf16 v[132:135], v[144:147], v[176:179], v[132:135]
	v_mfma_f32_16x16x32_bf16 v[128:131], v[162:165], v[176:179], v[128:131]
	v_mfma_f32_16x16x32_bf16 v[116:119], v[144:147], v[194:197], v[116:119]
	v_mfma_f32_16x16x32_bf16 v[112:115], v[162:165], v[194:197], v[112:115]
	v_mfma_f32_16x16x32_bf16 v[100:103], v[144:147], v[202:205], v[100:103]
	v_mfma_f32_16x16x32_bf16 v[96:99], v[162:165], v[202:205], v[96:99]
	v_mfma_f32_16x16x32_bf16 v[84:87], v[144:147], v[224:227], v[84:87]
	v_mfma_f32_16x16x32_bf16 v[80:83], v[162:165], v[224:227], v[80:83]
	v_mfma_f32_16x16x32_bf16 v[132:135], v[148:151], v[180:183], v[132:135]
	v_mfma_f32_16x16x32_bf16 v[128:131], v[172:175], v[180:183], v[128:131]
	v_mfma_f32_16x16x32_bf16 v[116:119], v[148:151], v[198:201], v[116:119]
	v_mfma_f32_16x16x32_bf16 v[112:115], v[172:175], v[198:201], v[112:115]
	v_mfma_f32_16x16x32_bf16 v[100:103], v[148:151], v[206:209], v[100:103]
	v_mfma_f32_16x16x32_bf16 v[96:99], v[172:175], v[206:209], v[96:99]
	v_mfma_f32_16x16x32_bf16 v[84:87], v[148:151], v[228:231], v[84:87]
	v_mfma_f32_16x16x32_bf16 v[80:83], v[172:175], v[228:231], v[80:83]
	s_setprio 0
	s_barrier
	s_add_i32 s28, s48, s46
	v_lshl_add_u64 v[166:167], v[166:167], 0, s[68:69]
	s_mov_b32 m0, s28
	ds_read_b128 v[176:179], v171 offset:49152
	ds_read_b128 v[180:183], v171 offset:50176
	ds_read_b128 v[194:197], v171 offset:51200
	ds_read_b128 v[198:201], v171 offset:52224
	ds_read_b128 v[202:205], v171 offset:53248
	ds_read_b128 v[206:209], v171 offset:54272
	ds_read_b128 v[224:227], v171 offset:55296
	ds_read_b128 v[228:231], v171 offset:56320
	global_load_lds_dwordx4 v[166:167], off
	s_add_i32 m0, s28, 0x2000
	s_add_u32 s28, s42, 0x80080
	v_lshl_add_u64 v[166:167], v[210:211], 0, s[68:69]
	s_addc_u32 s29, s43, 0
	s_add_i32 s42, s49, s46
	global_load_lds_dwordx4 v[166:167], off
	v_lshl_add_u64 v[166:167], s[28:29], 0, v[184:185]
	s_mov_b32 m0, s42
	s_nop 0
	global_load_lds_dwordx4 v[166:167], off
	v_lshl_add_u64 v[166:167], s[28:29], 0, v[152:153]
	s_add_i32 m0, s42, 0x2000
	s_nop 0
	global_load_lds_dwordx4 v[166:167], off
	v_lshl_add_u64 v[166:167], v[216:217], 0, s[68:69]
	s_mov_b32 m0, s53
	s_nop 0
	global_load_lds_dwordx4 v[166:167], off
	v_lshl_add_u64 v[166:167], v[218:219], 0, s[68:69]
	s_mov_b32 m0, s58
	s_nop 0
	global_load_lds_dwordx4 v[166:167], off
	s_waitcnt vmcnt(8)
	s_waitcnt lgkmcnt(0)
	s_barrier
	s_setprio 1
	s_waitcnt lgkmcnt(0)
	v_mfma_f32_16x16x32_bf16 v[76:79], v[56:59], v[176:179], v[76:79]
	v_mfma_f32_16x16x32_bf16 v[72:75], v[64:67], v[176:179], v[72:75]
	v_mfma_f32_16x16x32_bf16 v[52:55], v[56:59], v[194:197], v[52:55]
	v_mfma_f32_16x16x32_bf16 v[48:51], v[64:67], v[194:197], v[48:51]
	v_mfma_f32_16x16x32_bf16 v[28:31], v[56:59], v[202:205], v[28:31]
	v_mfma_f32_16x16x32_bf16 v[24:27], v[64:67], v[202:205], v[24:27]
	v_mfma_f32_16x16x32_bf16 v[12:15], v[56:59], v[224:227], v[12:15]
	v_mfma_f32_16x16x32_bf16 v[8:11], v[64:67], v[224:227], v[8:11]
	v_mfma_f32_16x16x32_bf16 v[76:79], v[60:63], v[180:183], v[76:79]
	v_mfma_f32_16x16x32_bf16 v[72:75], v[68:71], v[180:183], v[72:75]
	v_mfma_f32_16x16x32_bf16 v[52:55], v[60:63], v[198:201], v[52:55]
	v_mfma_f32_16x16x32_bf16 v[48:51], v[68:71], v[198:201], v[48:51]
	v_mfma_f32_16x16x32_bf16 v[28:31], v[60:63], v[206:209], v[28:31]
	v_mfma_f32_16x16x32_bf16 v[24:27], v[68:71], v[206:209], v[24:27]
	v_mfma_f32_16x16x32_bf16 v[12:15], v[60:63], v[228:231], v[12:15]
	v_mfma_f32_16x16x32_bf16 v[8:11], v[68:71], v[228:231], v[8:11]
	s_setprio 0
	s_setprio 1
	v_mfma_f32_16x16x32_bf16 v[40:43], v[144:147], v[176:179], v[40:43]
	v_mfma_f32_16x16x32_bf16 v[68:71], v[148:151], v[180:183], v[40:43]
	v_mfma_f32_16x16x32_bf16 v[40:43], v[162:165], v[176:179], v[44:47]
	v_mfma_f32_16x16x32_bf16 v[36:39], v[144:147], v[194:197], v[36:39]
	v_mfma_f32_16x16x32_bf16 v[32:35], v[162:165], v[194:197], v[32:35]
	v_mfma_f32_16x16x32_bf16 v[20:23], v[144:147], v[202:205], v[20:23]
	v_mfma_f32_16x16x32_bf16 v[16:19], v[162:165], v[202:205], v[16:19]
	v_mfma_f32_16x16x32_bf16 v[4:7], v[144:147], v[224:227], v[4:7]
	v_mfma_f32_16x16x32_bf16 v[0:3], v[162:165], v[224:227], v[0:3]
	v_mfma_f32_16x16x32_bf16 v[64:67], v[172:175], v[180:183], v[40:43]
	v_mfma_f32_16x16x32_bf16 v[36:39], v[148:151], v[198:201], v[36:39]
	v_mfma_f32_16x16x32_bf16 v[32:35], v[172:175], v[198:201], v[32:35]
	v_mfma_f32_16x16x32_bf16 v[20:23], v[148:151], v[206:209], v[20:23]
	v_mfma_f32_16x16x32_bf16 v[16:19], v[172:175], v[206:209], v[16:19]
	v_mfma_f32_16x16x32_bf16 v[4:7], v[148:151], v[228:231], v[4:7]
	v_mfma_f32_16x16x32_bf16 v[0:3], v[172:175], v[228:231], v[0:3]
	s_setprio 0
	s_barrier
	s_add_i32 s79, s79, 2
	s_add_u32 s40, s40, 0x100
	s_addc_u32 s41, s41, 0
	s_add_u32 s62, s62, 0x100
	s_addc_u32 s63, s63, 0
	s_cmp_gt_u32 s79, 29
	s_cbranch_scc0 .LBB0_991
	s_and_b64 vcc, exec, s[8:9]
	s_cbranch_vccz .LBB0_994
	s_barrier

.LBB0_1660:
	v_readlane_b32 s14, v253, 45
	v_readlane_b32 s15, v253, 46
	s_add_u32 s14, s14, s10
	s_addc_u32 s15, s15, s11
	s_and_b64 s[16:17], s[36:37], exec
	v_readlane_b32 s16, v253, 39
	s_cselect_b32 s51, s15, s19
	s_cselect_b32 s52, s14, s18
	s_add_u32 s16, s16, s12
	v_readlane_b32 s17, v253, 40
	s_addc_u32 s17, s17, s13
	s_and_b64 s[28:29], s[36:37], exec
	s_cselect_b32 s53, s17, s25
	s_cselect_b32 s58, s16, s24
	s_add_u32 s59, s24, 0x100
	v_mov_b32_e32 v0, 0
	s_addc_u32 s60, s25, 0
	s_mov_b32 s61, -2
	v_mov_b32_e32 v1, v0
	v_mov_b32_e32 v2, v0
	v_mov_b32_e32 v3, v0
	v_mov_b32_e32 v4, v0
	v_mov_b32_e32 v5, v0
	v_mov_b32_e32 v6, v0
	v_mov_b32_e32 v7, v0
	v_mov_b32_e32 v16, v0
	v_mov_b32_e32 v17, v0
	v_mov_b32_e32 v18, v0
	v_mov_b32_e32 v19, v0
	v_mov_b32_e32 v20, v0
	v_mov_b32_e32 v21, v0
	v_mov_b32_e32 v22, v0
	v_mov_b32_e32 v23, v0
	v_mov_b32_e32 v32, v0
	v_mov_b32_e32 v33, v0
	v_mov_b32_e32 v34, v0
	v_mov_b32_e32 v35, v0
	v_mov_b32_e32 v36, v0
	v_mov_b32_e32 v37, v0
	v_mov_b32_e32 v38, v0
	v_mov_b32_e32 v39, v0
	v_mov_b32_e32 v48, v0
	v_mov_b32_e32 v49, v0
	v_mov_b32_e32 v50, v0
	v_mov_b32_e32 v51, v0
	v_mov_b32_e32 v52, v0
	v_mov_b32_e32 v53, v0
	v_mov_b32_e32 v54, v0
	v_mov_b32_e32 v55, v0
	v_mov_b32_e32 v8, v0
	v_mov_b32_e32 v9, v0
	v_mov_b32_e32 v10, v0
	v_mov_b32_e32 v11, v0
	v_mov_b32_e32 v12, v0
	v_mov_b32_e32 v13, v0
	v_mov_b32_e32 v14, v0
	v_mov_b32_e32 v15, v0
	v_mov_b32_e32 v24, v0
	v_mov_b32_e32 v25, v0
	v_mov_b32_e32 v26, v0
	v_mov_b32_e32 v27, v0
	v_mov_b32_e32 v28, v0
	v_mov_b32_e32 v29, v0
	v_mov_b32_e32 v30, v0
	v_mov_b32_e32 v31, v0
	v_mov_b32_e32 v40, v0
	v_mov_b32_e32 v41, v0
	v_mov_b32_e32 v42, v0
	v_mov_b32_e32 v43, v0
	v_mov_b32_e32 v44, v0
	v_mov_b32_e32 v45, v0
	v_mov_b32_e32 v46, v0
	v_mov_b32_e32 v47, v0
	v_mov_b32_e32 v56, v0
	v_mov_b32_e32 v57, v0
	v_mov_b32_e32 v58, v0
	v_mov_b32_e32 v59, v0
	v_mov_b32_e32 v60, v0
	v_mov_b32_e32 v61, v0
	v_mov_b32_e32 v62, v0
	v_mov_b32_e32 v63, v0
	v_mov_b32_e32 v72, v0
	v_mov_b32_e32 v73, v0
	v_mov_b32_e32 v74, v0
	v_mov_b32_e32 v75, v0
	v_mov_b32_e32 v76, v0
	v_mov_b32_e32 v77, v0
	v_mov_b32_e32 v78, v0
	v_mov_b32_e32 v79, v0
	v_mov_b32_e32 v96, v0
	v_mov_b32_e32 v97, v0
	v_mov_b32_e32 v98, v0
	v_mov_b32_e32 v99, v0
	v_mov_b32_e32 v100, v0
	v_mov_b32_e32 v101, v0
	v_mov_b32_e32 v102, v0
	v_mov_b32_e32 v103, v0
	v_mov_b32_e32 v112, v0
	v_mov_b32_e32 v113, v0
	v_mov_b32_e32 v114, v0
	v_mov_b32_e32 v115, v0
	v_mov_b32_e32 v116, v0
	v_mov_b32_e32 v117, v0
	v_mov_b32_e32 v118, v0
	v_mov_b32_e32 v119, v0
	v_mov_b32_e32 v128, v0
	v_mov_b32_e32 v129, v0
	v_mov_b32_e32 v130, v0
	v_mov_b32_e32 v131, v0
	v_mov_b32_e32 v132, v0
	v_mov_b32_e32 v133, v0
	v_mov_b32_e32 v134, v0
	v_mov_b32_e32 v135, v0
	v_mov_b32_e32 v88, v0
	v_mov_b32_e32 v89, v0
	v_mov_b32_e32 v90, v0
	v_mov_b32_e32 v91, v0
	v_mov_b32_e32 v92, v0
	v_mov_b32_e32 v93, v0
	v_mov_b32_e32 v94, v0
	v_mov_b32_e32 v95, v0
	v_mov_b32_e32 v104, v0
	v_mov_b32_e32 v105, v0
	v_mov_b32_e32 v106, v0
	v_mov_b32_e32 v107, v0
	v_mov_b32_e32 v108, v0
	v_mov_b32_e32 v109, v0
	v_mov_b32_e32 v110, v0
	v_mov_b32_e32 v111, v0
	v_mov_b32_e32 v120, v0
	v_mov_b32_e32 v121, v0
	v_mov_b32_e32 v122, v0
	v_mov_b32_e32 v123, v0
	v_mov_b32_e32 v124, v0
	v_mov_b32_e32 v125, v0
	v_mov_b32_e32 v126, v0
	v_mov_b32_e32 v127, v0
	v_mov_b32_e32 v136, v0
	v_mov_b32_e32 v137, v0
	v_mov_b32_e32 v138, v0
	v_mov_b32_e32 v139, v0
	v_mov_b32_e32 v140, v0
	v_mov_b32_e32 v141, v0
	v_mov_b32_e32 v142, v0
	v_mov_b32_e32 v143, v0
	s_waitcnt vmcnt(0)
.LBB0_1661:
	s_add_u32 s24, s18, 0x100
	s_addc_u32 s25, s19, 0
	s_add_i32 s28, 0, 0x10000
	s_cmpk_eq_i32 s61, 0x54
	s_cselect_b32 s39, s51, s25
	s_cselect_b32 s38, s52, s24
	s_cselect_b32 s31, s53, s60
	s_cselect_b32 s30, s58, s59
	s_add_i32 s29, 0, 0x14000
	v_add_u32_e32 v84, s28, v163
	v_add_u32_e32 v170, s29, v163
	ds_read_b128 v[64:67], v84
	ds_read_b128 v[68:71], v84 offset:1024
	ds_read_b128 v[80:83], v84 offset:2048
	ds_read_b128 v[84:87], v84 offset:3072
	ds_read_b128 v[154:157], v170
	ds_read_b128 v[158:161], v170 offset:1024
	ds_read_b128 v[166:169], v170 offset:2048
	ds_read_b128 v[170:173], v170 offset:3072
	v_lshl_add_u64 v[182:183], s[18:19], 0, v[150:151]
	s_add_i32 m0, s20, 0xc000
	ds_read_b128 v[174:177], v165
	ds_read_b128 v[178:181], v165 offset:1024
	ds_read_b128 v[194:197], v165 offset:2048
	ds_read_b128 v[198:201], v165 offset:3072
	ds_read_b128 v[202:205], v165 offset:4096
	ds_read_b128 v[206:209], v165 offset:5120
	ds_read_b128 v[224:227], v165 offset:6144
	ds_read_b128 v[228:231], v165 offset:7168
	global_load_lds_dwordx4 v[182:183], off
	v_lshl_add_u64 v[182:183], s[18:19], 0, v[152:153]
	s_add_i32 m0, s20, 0xe000
	s_nop 0
	global_load_lds_dwordx4 v[182:183], off
	s_waitcnt vmcnt(8)
	s_waitcnt lgkmcnt(0)
	s_barrier
	s_setprio 1
	s_waitcnt lgkmcnt(0)
	v_mfma_f32_16x16x32_bf16 v[140:143], v[64:67], v[174:177], v[140:143]
	v_mfma_f32_16x16x32_bf16 v[136:139], v[80:83], v[174:177], v[136:139]
	v_mfma_f32_16x16x32_bf16 v[124:127], v[64:67], v[194:197], v[124:127]
	v_mfma_f32_16x16x32_bf16 v[120:123], v[80:83], v[194:197], v[120:123]
	v_mfma_f32_16x16x32_bf16 v[108:111], v[64:67], v[202:205], v[108:111]
	v_mfma_f32_16x16x32_bf16 v[104:107], v[80:83], v[202:205], v[104:107]
	v_mfma_f32_16x16x32_bf16 v[92:95], v[64:67], v[224:227], v[92:95]
	v_mfma_f32_16x16x32_bf16 v[88:91], v[80:83], v[224:227], v[88:91]
	v_mfma_f32_16x16x32_bf16 v[140:143], v[68:71], v[178:181], v[140:143]
	v_mfma_f32_16x16x32_bf16 v[136:139], v[84:87], v[178:181], v[136:139]
	v_mfma_f32_16x16x32_bf16 v[124:127], v[68:71], v[198:201], v[124:127]
	v_mfma_f32_16x16x32_bf16 v[120:123], v[84:87], v[198:201], v[120:123]
	v_mfma_f32_16x16x32_bf16 v[108:111], v[68:71], v[206:209], v[108:111]
	v_mfma_f32_16x16x32_bf16 v[104:107], v[84:87], v[206:209], v[104:107]
	v_mfma_f32_16x16x32_bf16 v[92:95], v[68:71], v[228:231], v[92:95]
	v_mfma_f32_16x16x32_bf16 v[88:91], v[84:87], v[228:231], v[88:91]
	s_setprio 0
	s_setprio 1
	v_mfma_f32_16x16x32_bf16 v[132:135], v[154:157], v[174:177], v[132:135]
	v_mfma_f32_16x16x32_bf16 v[128:131], v[166:169], v[174:177], v[128:131]
	v_mfma_f32_16x16x32_bf16 v[116:119], v[154:157], v[194:197], v[116:119]
	v_mfma_f32_16x16x32_bf16 v[112:115], v[166:169], v[194:197], v[112:115]
	v_mfma_f32_16x16x32_bf16 v[100:103], v[154:157], v[202:205], v[100:103]
	v_mfma_f32_16x16x32_bf16 v[96:99], v[166:169], v[202:205], v[96:99]
	v_mfma_f32_16x16x32_bf16 v[76:79], v[154:157], v[224:227], v[76:79]
	v_mfma_f32_16x16x32_bf16 v[72:75], v[166:169], v[224:227], v[72:75]
	v_mfma_f32_16x16x32_bf16 v[132:135], v[158:161], v[178:181], v[132:135]
	v_mfma_f32_16x16x32_bf16 v[128:131], v[170:173], v[178:181], v[128:131]
	v_mfma_f32_16x16x32_bf16 v[116:119], v[158:161], v[198:201], v[116:119]
	v_mfma_f32_16x16x32_bf16 v[112:115], v[170:173], v[198:201], v[112:115]
	v_mfma_f32_16x16x32_bf16 v[100:103], v[158:161], v[206:209], v[100:103]
	v_mfma_f32_16x16x32_bf16 v[96:99], v[170:173], v[206:209], v[96:99]
	v_mfma_f32_16x16x32_bf16 v[76:79], v[158:161], v[228:231], v[76:79]
	v_mfma_f32_16x16x32_bf16 v[72:75], v[170:173], v[228:231], v[72:75]
	s_setprio 0
	s_barrier
	s_add_i32 s18, s28, s4
	v_lshl_add_u64 v[182:183], s[30:31], 0, v[184:185]
	s_mov_b32 m0, s18
	ds_read_b128 v[174:177], v165 offset:16384
	ds_read_b128 v[178:181], v165 offset:17408
	ds_read_b128 v[194:197], v165 offset:18432
	ds_read_b128 v[198:201], v165 offset:19456
	ds_read_b128 v[202:205], v165 offset:20480
	ds_read_b128 v[206:209], v165 offset:21504
	ds_read_b128 v[224:227], v165 offset:22528
	ds_read_b128 v[228:231], v165 offset:23552
	global_load_lds_dwordx4 v[182:183], off
	s_add_i32 m0, s18, 0x2000
	s_add_u32 s18, s30, 0x160000
	v_lshl_add_u64 v[210:211], s[30:31], 0, v[144:145]
	s_addc_u32 s19, s31, 0
	s_add_i32 s28, s29, s4
	global_load_lds_dwordx4 v[210:211], off
	v_lshl_add_u64 v[216:217], s[18:19], 0, v[184:185]
	s_mov_b32 m0, s28
	v_lshl_add_u64 v[218:219], s[38:39], 0, v[146:147]
	global_load_lds_dwordx4 v[216:217], off
	v_lshl_add_u64 v[216:217], s[18:19], 0, v[144:145]
	s_add_i32 m0, s28, 0x2000
	s_nop 0
	global_load_lds_dwordx4 v[216:217], off
	v_lshl_add_u64 v[216:217], s[38:39], 0, v[148:149]
	s_mov_b32 m0, s20
	s_nop 0
	global_load_lds_dwordx4 v[216:217], off
	s_mov_b32 m0, s21
	s_nop 0
	global_load_lds_dwordx4 v[218:219], off
	s_waitcnt vmcnt(8)
	s_waitcnt lgkmcnt(0)
	s_barrier
	s_setprio 1
	s_waitcnt lgkmcnt(0)
	v_mfma_f32_16x16x32_bf16 v[60:63], v[64:67], v[174:177], v[60:63]
	v_mfma_f32_16x16x32_bf16 v[56:59], v[80:83], v[174:177], v[56:59]
	v_mfma_f32_16x16x32_bf16 v[44:47], v[64:67], v[194:197], v[44:47]
	v_mfma_f32_16x16x32_bf16 v[40:43], v[80:83], v[194:197], v[40:43]
	v_mfma_f32_16x16x32_bf16 v[28:31], v[64:67], v[202:205], v[28:31]
	v_mfma_f32_16x16x32_bf16 v[24:27], v[80:83], v[202:205], v[24:27]
	v_mfma_f32_16x16x32_bf16 v[12:15], v[64:67], v[224:227], v[12:15]
	v_mfma_f32_16x16x32_bf16 v[8:11], v[80:83], v[224:227], v[8:11]
	v_mfma_f32_16x16x32_bf16 v[60:63], v[68:71], v[178:181], v[60:63]
	v_mfma_f32_16x16x32_bf16 v[56:59], v[84:87], v[178:181], v[56:59]
	v_mfma_f32_16x16x32_bf16 v[44:47], v[68:71], v[198:201], v[44:47]
	v_mfma_f32_16x16x32_bf16 v[40:43], v[84:87], v[198:201], v[40:43]
	v_mfma_f32_16x16x32_bf16 v[28:31], v[68:71], v[206:209], v[28:31]
	v_mfma_f32_16x16x32_bf16 v[24:27], v[84:87], v[206:209], v[24:27]
	v_mfma_f32_16x16x32_bf16 v[12:15], v[68:71], v[228:231], v[12:15]
	v_mfma_f32_16x16x32_bf16 v[8:11], v[84:87], v[228:231], v[8:11]
	s_setprio 0
	s_setprio 1
	v_mfma_f32_16x16x32_bf16 v[52:55], v[154:157], v[174:177], v[52:55]
	v_mfma_f32_16x16x32_bf16 v[48:51], v[166:169], v[174:177], v[48:51]
	v_mfma_f32_16x16x32_bf16 v[36:39], v[154:157], v[194:197], v[36:39]
	v_mfma_f32_16x16x32_bf16 v[32:35], v[166:169], v[194:197], v[32:35]
	v_mfma_f32_16x16x32_bf16 v[20:23], v[154:157], v[202:205], v[20:23]
	v_mfma_f32_16x16x32_bf16 v[16:19], v[166:169], v[202:205], v[16:19]
	v_mfma_f32_16x16x32_bf16 v[4:7], v[154:157], v[224:227], v[4:7]
	v_mfma_f32_16x16x32_bf16 v[0:3], v[166:169], v[224:227], v[0:3]
	v_mfma_f32_16x16x32_bf16 v[52:55], v[158:161], v[178:181], v[52:55]
	v_mfma_f32_16x16x32_bf16 v[48:51], v[170:173], v[178:181], v[48:51]
	v_mfma_f32_16x16x32_bf16 v[36:39], v[158:161], v[198:201], v[36:39]
	v_mfma_f32_16x16x32_bf16 v[32:35], v[170:173], v[198:201], v[32:35]
	v_mfma_f32_16x16x32_bf16 v[20:23], v[158:161], v[206:209], v[20:23]
	v_mfma_f32_16x16x32_bf16 v[16:19], v[170:173], v[206:209], v[16:19]
	v_mfma_f32_16x16x32_bf16 v[4:7], v[158:161], v[228:231], v[4:7]
	v_mfma_f32_16x16x32_bf16 v[0:3], v[170:173], v[228:231], v[0:3]
	s_setprio 0
	s_barrier
	s_add_i32 s28, 0, 0x18000
	s_add_i32 s29, 0, 0x1c000
	v_add_u32_e32 v84, s28, v163
	v_add_u32_e32 v170, s29, v163
	ds_read_b128 v[64:67], v84
	ds_read_b128 v[68:71], v84 offset:1024
	ds_read_b128 v[80:83], v84 offset:2048
	ds_read_b128 v[84:87], v84 offset:3072
	ds_read_b128 v[154:157], v170
	ds_read_b128 v[158:161], v170 offset:1024
	ds_read_b128 v[166:169], v170 offset:2048
	ds_read_b128 v[170:173], v170 offset:3072
	s_add_u32 s18, s38, 0x160000
	s_addc_u32 s19, s39, 0
	s_mov_b32 m0, s26
	v_lshl_add_u64 v[232:233], s[18:19], 0, v[148:149]
	ds_read_b128 v[174:177], v165 offset:32768
	ds_read_b128 v[178:181], v165 offset:33792
	ds_read_b128 v[194:197], v165 offset:34816
	ds_read_b128 v[198:201], v165 offset:35840
	ds_read_b128 v[202:205], v165 offset:36864
	ds_read_b128 v[206:209], v165 offset:37888
	ds_read_b128 v[224:227], v165 offset:38912
	ds_read_b128 v[228:231], v165 offset:39936
	global_load_lds_dwordx4 v[232:233], off
	v_lshl_add_u64 v[232:233], s[18:19], 0, v[146:147]
	s_mov_b32 m0, s27
	s_nop 0
	global_load_lds_dwordx4 v[232:233], off
	s_waitcnt vmcnt(8)
	s_waitcnt lgkmcnt(0)
	s_barrier
	s_setprio 1
	s_waitcnt lgkmcnt(0)
	v_mfma_f32_16x16x32_bf16 v[140:143], v[64:67], v[174:177], v[140:143]
	v_mfma_f32_16x16x32_bf16 v[136:139], v[80:83], v[174:177], v[136:139]
	v_mfma_f32_16x16x32_bf16 v[124:127], v[64:67], v[194:197], v[124:127]
	v_mfma_f32_16x16x32_bf16 v[120:123], v[80:83], v[194:197], v[120:123]
	v_mfma_f32_16x16x32_bf16 v[108:111], v[64:67], v[202:205], v[108:111]
	v_mfma_f32_16x16x32_bf16 v[104:107], v[80:83], v[202:205], v[104:107]
	v_mfma_f32_16x16x32_bf16 v[92:95], v[64:67], v[224:227], v[92:95]
	v_mfma_f32_16x16x32_bf16 v[88:91], v[80:83], v[224:227], v[88:91]
	v_mfma_f32_16x16x32_bf16 v[140:143], v[68:71], v[178:181], v[140:143]
	v_mfma_f32_16x16x32_bf16 v[136:139], v[84:87], v[178:181], v[136:139]
	v_mfma_f32_16x16x32_bf16 v[124:127], v[68:71], v[198:201], v[124:127]
	v_mfma_f32_16x16x32_bf16 v[120:123], v[84:87], v[198:201], v[120:123]
	v_mfma_f32_16x16x32_bf16 v[108:111], v[68:71], v[206:209], v[108:111]
	v_mfma_f32_16x16x32_bf16 v[104:107], v[84:87], v[206:209], v[104:107]
	v_mfma_f32_16x16x32_bf16 v[92:95], v[68:71], v[228:231], v[92:95]
	v_mfma_f32_16x16x32_bf16 v[88:91], v[84:87], v[228:231], v[88:91]
	s_setprio 0
	s_setprio 1
	v_mfma_f32_16x16x32_bf16 v[132:135], v[154:157], v[174:177], v[132:135]
	v_mfma_f32_16x16x32_bf16 v[128:131], v[166:169], v[174:177], v[128:131]
	v_mfma_f32_16x16x32_bf16 v[116:119], v[154:157], v[194:197], v[116:119]
	v_mfma_f32_16x16x32_bf16 v[112:115], v[166:169], v[194:197], v[112:115]
	v_mfma_f32_16x16x32_bf16 v[100:103], v[154:157], v[202:205], v[100:103]
	v_mfma_f32_16x16x32_bf16 v[96:99], v[166:169], v[202:205], v[96:99]
	v_mfma_f32_16x16x32_bf16 v[76:79], v[154:157], v[224:227], v[76:79]
	v_mfma_f32_16x16x32_bf16 v[72:75], v[166:169], v[224:227], v[72:75]
	v_mfma_f32_16x16x32_bf16 v[132:135], v[158:161], v[178:181], v[132:135]
	v_mfma_f32_16x16x32_bf16 v[128:131], v[170:173], v[178:181], v[128:131]
	v_mfma_f32_16x16x32_bf16 v[116:119], v[158:161], v[198:201], v[116:119]
	v_mfma_f32_16x16x32_bf16 v[112:115], v[170:173], v[198:201], v[112:115]
	v_mfma_f32_16x16x32_bf16 v[100:103], v[158:161], v[206:209], v[100:103]
	v_mfma_f32_16x16x32_bf16 v[96:99], v[170:173], v[206:209], v[96:99]
	v_mfma_f32_16x16x32_bf16 v[76:79], v[158:161], v[228:231], v[76:79]
	v_mfma_f32_16x16x32_bf16 v[72:75], v[170:173], v[228:231], v[72:75]
	s_setprio 0
	s_barrier
	s_add_i32 s18, s28, s4
	v_lshl_add_u64 v[182:183], v[182:183], 0, s[68:69]
	s_mov_b32 m0, s18
	ds_read_b128 v[174:177], v165 offset:49152
	ds_read_b128 v[178:181], v165 offset:50176
	ds_read_b128 v[194:197], v165 offset:51200
	ds_read_b128 v[198:201], v165 offset:52224
	ds_read_b128 v[202:205], v165 offset:53248
	ds_read_b128 v[206:209], v165 offset:54272
	ds_read_b128 v[224:227], v165 offset:55296
	ds_read_b128 v[228:231], v165 offset:56320
	global_load_lds_dwordx4 v[182:183], off
	s_add_i32 m0, s18, 0x2000
	s_add_u32 s18, s30, 0x160080
	v_lshl_add_u64 v[182:183], v[210:211], 0, s[68:69]
	s_addc_u32 s19, s31, 0
	s_add_i32 s28, s29, s4
	global_load_lds_dwordx4 v[182:183], off
	v_lshl_add_u64 v[182:183], s[18:19], 0, v[184:185]
	s_mov_b32 m0, s28
	s_nop 0
	global_load_lds_dwordx4 v[182:183], off
	v_lshl_add_u64 v[182:183], s[18:19], 0, v[144:145]
	s_add_i32 m0, s28, 0x2000
	s_nop 0
	global_load_lds_dwordx4 v[182:183], off
	v_lshl_add_u64 v[182:183], v[216:217], 0, s[68:69]
	s_mov_b32 m0, s42
	s_nop 0
	global_load_lds_dwordx4 v[182:183], off
	v_lshl_add_u64 v[182:183], v[218:219], 0, s[68:69]
	s_mov_b32 m0, s43
	s_nop 0
	global_load_lds_dwordx4 v[182:183], off
	s_waitcnt vmcnt(8)
	s_waitcnt lgkmcnt(0)
	s_barrier
	s_setprio 1
	s_waitcnt lgkmcnt(0)
	v_mfma_f32_16x16x32_bf16 v[60:63], v[64:67], v[174:177], v[60:63]
	v_mfma_f32_16x16x32_bf16 v[56:59], v[80:83], v[174:177], v[56:59]
	v_mfma_f32_16x16x32_bf16 v[44:47], v[64:67], v[194:197], v[44:47]
	v_mfma_f32_16x16x32_bf16 v[40:43], v[80:83], v[194:197], v[40:43]
	v_mfma_f32_16x16x32_bf16 v[28:31], v[64:67], v[202:205], v[28:31]
	v_mfma_f32_16x16x32_bf16 v[24:27], v[80:83], v[202:205], v[24:27]
	v_mfma_f32_16x16x32_bf16 v[12:15], v[64:67], v[224:227], v[12:15]
	v_mfma_f32_16x16x32_bf16 v[8:11], v[80:83], v[224:227], v[8:11]
	v_mfma_f32_16x16x32_bf16 v[60:63], v[68:71], v[178:181], v[60:63]
	v_mfma_f32_16x16x32_bf16 v[56:59], v[84:87], v[178:181], v[56:59]
	v_mfma_f32_16x16x32_bf16 v[44:47], v[68:71], v[198:201], v[44:47]
	v_mfma_f32_16x16x32_bf16 v[40:43], v[84:87], v[198:201], v[40:43]
	v_mfma_f32_16x16x32_bf16 v[28:31], v[68:71], v[206:209], v[28:31]
	v_mfma_f32_16x16x32_bf16 v[24:27], v[84:87], v[206:209], v[24:27]
	v_mfma_f32_16x16x32_bf16 v[12:15], v[68:71], v[228:231], v[12:15]
	v_mfma_f32_16x16x32_bf16 v[8:11], v[84:87], v[228:231], v[8:11]
	s_setprio 0
	s_setprio 1
	v_mfma_f32_16x16x32_bf16 v[52:55], v[154:157], v[174:177], v[52:55]
	v_mfma_f32_16x16x32_bf16 v[48:51], v[166:169], v[174:177], v[48:51]
	v_mfma_f32_16x16x32_bf16 v[36:39], v[154:157], v[194:197], v[36:39]
	v_mfma_f32_16x16x32_bf16 v[32:35], v[166:169], v[194:197], v[32:35]
	v_mfma_f32_16x16x32_bf16 v[20:23], v[154:157], v[202:205], v[20:23]
	v_mfma_f32_16x16x32_bf16 v[16:19], v[166:169], v[202:205], v[16:19]
	v_mfma_f32_16x16x32_bf16 v[4:7], v[154:157], v[224:227], v[4:7]
	v_mfma_f32_16x16x32_bf16 v[0:3], v[166:169], v[224:227], v[0:3]
	v_mfma_f32_16x16x32_bf16 v[52:55], v[158:161], v[178:181], v[52:55]
	v_mfma_f32_16x16x32_bf16 v[48:51], v[170:173], v[178:181], v[48:51]
	v_mfma_f32_16x16x32_bf16 v[36:39], v[158:161], v[198:201], v[36:39]
	v_mfma_f32_16x16x32_bf16 v[32:35], v[170:173], v[198:201], v[32:35]
	v_mfma_f32_16x16x32_bf16 v[20:23], v[158:161], v[206:209], v[20:23]
	v_mfma_f32_16x16x32_bf16 v[16:19], v[170:173], v[206:209], v[16:19]
	v_mfma_f32_16x16x32_bf16 v[4:7], v[158:161], v[228:231], v[4:7]
	v_mfma_f32_16x16x32_bf16 v[0:3], v[170:173], v[228:231], v[0:3]
	s_setprio 0
	s_barrier
	s_add_i32 s61, s61, 2
	s_add_u32 s59, s59, 0x100
	s_addc_u32 s60, s60, 0
	s_cmpk_gt_u32 s61, 0x55
	s_mov_b64 s[18:19], s[24:25]
	s_cbranch_scc0 .LBB0_1661
	s_and_b64 vcc, exec, s[8:9]
	s_cbranch_vccz .LBB0_1664
	s_barrier
